# P3 mLSTM prep: the four serialized V^T staging loads issued together with counted waits
# baseline (speedup 1.0000x reference)
.LBB0_347:
	s_cmpk_lt_i32 s51, 0x80
	s_cselect_b64 s[34:35], -1, 0
	s_cmpk_gt_i32 s51, 0x7f
	s_cselect_b64 s[16:17], -1, 0
	s_and_b64 s[4:5], s[16:17], exec
	v_add_u32_e32 v172, s36, v188
	s_waitcnt lgkmcnt(0)
	v_mov_b64_e32 v[2:3], s[58:59]
	s_cselect_b32 s37, 0x4000, 0
	v_mad_i64_i32 v[2:3], s[4:5], v172, s43, v[2:3]
	s_lshl_b32 s22, s52, 8
	v_lshl_add_u64 v[2:3], v[2:3], 0, s[22:23]
	v_mov_b32_e32 v163, v147
	v_lshl_add_u64 v[2:3], v[2:3], 0, v[162:163]
	s_mov_b64 s[4:5], 0x1eb00400
	v_lshl_add_u64 v[6:7], v[2:3], 0, s[4:5]
	s_mov_b32 s4, 0x1eb00000
	v_add_co_u32_e32 v2, vcc, s4, v2
	s_lshl_b32 s22, s52, 6
	s_nop 0
	v_addc_co_u32_e32 v3, vcc, 0, v3, vcc
	global_load_dwordx4 v[2:5], v[2:3], off offset:1024
	global_load_dwordx4 v[208:211], v[6:7], off offset:16
	global_load_dwordx4 v[212:215], v[6:7], off offset:32
	global_load_dwordx4 v[216:219], v[6:7], off offset:48
	v_cmp_lt_i32_e64 s[4:5], s37, v172
	v_mov_b32_e32 v102, 0
	v_mov_b32_e32 v46, 0
	v_mov_b32_e32 v47, 0
	v_mov_b32_e32 v48, 0
	v_mov_b32_e32 v49, 0
	s_waitcnt vmcnt(3)
	ds_write_b16 v189, v2
	ds_write_b16_d16_hi v189, v2 offset:272
	ds_write_b16 v189, v3 offset:544
	ds_write_b16_d16_hi v189, v3 offset:816
	ds_write_b16 v189, v4 offset:1088
	ds_write_b16_d16_hi v189, v4 offset:1360
	ds_write_b16 v189, v5 offset:1632
	ds_write_b16_d16_hi v189, v5 offset:1904
	s_waitcnt vmcnt(2)
	ds_write_b16 v190, v208
	ds_write_b16_d16_hi v190, v208 offset:272
	ds_write_b16 v189, v209 offset:2720
	ds_write_b16_d16_hi v189, v209 offset:2992
	ds_write_b16 v189, v210 offset:3264
	ds_write_b16_d16_hi v189, v210 offset:3536
	ds_write_b16 v189, v211 offset:3808
	ds_write_b16_d16_hi v189, v211 offset:4080
	s_waitcnt vmcnt(1)
	ds_write_b16 v191, v212
	ds_write_b16_d16_hi v191, v212 offset:272
	ds_write_b16 v189, v213 offset:4896
	ds_write_b16_d16_hi v189, v213 offset:5168
	ds_write_b16 v189, v214 offset:5440
	ds_write_b16_d16_hi v189, v214 offset:5712
	ds_write_b16 v189, v215 offset:5984
	ds_write_b16_d16_hi v189, v215 offset:6256
	v_or_b32_e32 v6, s22, v193
	v_lshlrev_b32_e32 v146, 1, v6
	v_add_u32_e32 v7, -1, v172
	s_waitcnt vmcnt(0)
	ds_write_b16 v192, v216
	ds_write_b16_d16_hi v192, v216 offset:272
	ds_write_b16 v189, v217 offset:7072
	ds_write_b16_d16_hi v189, v217 offset:7344
	ds_write_b16 v189, v218 offset:7616
	ds_write_b16_d16_hi v189, v218 offset:7888
	ds_write_b16 v189, v219 offset:8160
	ds_write_b16_d16_hi v189, v219 offset:8432
	v_mov_b64_e32 v[2:3], s[20:21]
	v_mad_i64_i32 v[4:5], s[36:37], v172, s43, v[2:3]
	v_lshl_add_u64 v[4:5], v[4:5], 0, v[146:147]
	s_waitcnt lgkmcnt(0)
	s_barrier
	global_load_dwordx4 v[42:45], v[4:5], off
	v_mad_u64_u32 v[2:3], s[36:37], v7, s43, v[2:3]
	v_lshl_add_u64 v[10:11], v[2:3], 0, v[146:147]
	s_and_saveexec_b64 s[36:37], s[4:5]
	s_cbranch_execz .LBB0_349
	global_load_dwordx4 v[46:49], v[10:11], off
